# GLA prep: next chunk's loads issued one full iteration ahead (gate tile ping-pong in two register sets, q/k loads re-issued per 16-column group right after consumption, counted vmcnt)
# speedup vs baseline: 1.0048x; 1.0004x over previous
; __device__ __forceinline__ void gla_fast_unit(int unit, const bf16_t* P, const float* w_up, const float* b_up, float* Of, float* Ob, LAS unsigned char* lds0) {
;     ...
;         u32x4 graw0; unsigned short qr0[4][4], kr0[4][4]; u32x4 vraw0[4];
;         const unsigned goff = (unsigned)((dir ? 63 - (16 * pw + l15) : 16 * pw + l15) * (LDP1 * 2) + (6144 + dir * 16 + 8 * q) * 2);
;         unsigned qkoff[4], voff[4];
; #pragma unroll
;         for (int r = 0; r < 4; ++r) { const int p = 16 * pw + 4 * q + r; qkoff[r] = (unsigned)((dir ? 63 - p : p) * (LDP1 * 2) + (h * 64 + l15) * 2); }
; #pragma unroll
;         for (int i = 0; i < 4; ++i) { const int piece = ptid + 256 * i, p = piece >> 4, ch = piece & 15; voff[i] = (unsigned)((dir ? 63 - p : p) * (LDP1 * 2) + (5120 + h * 128 + 8 * ch) * 2); }
;     ...
;         GLA_LOAD(0, graw0, qr0, kr0, vraw0);
.LBB0_1142:
	s_or_b64 exec, exec, s[8:9]
	v_mov_b32_e32 v250, 0
	v_mov_b32_e32 v251, 0
	v_mov_b32_e32 v252, 0
	v_mov_b32_e32 v253, 0
	v_or_b32_e32 v133, s13, v169
	v_lshlrev_b32_e32 v132, 1, v1
	v_sub_u32_e32 v11, 63, v133
	v_or_b32_e32 v12, s31, v132
	v_cndmask_b32_e64 v11, v11, v133, s[4:5]
	v_mad_u64_u32 v[16:17], s[8:9], v11, s11, v[12:13]
	v_or_b32_e32 v11, 1, v133
	v_sub_u32_e32 v13, 63, v11
	v_cndmask_b32_e64 v11, v13, v11, s[4:5]
	v_mad_u64_u32 v[28:29], s[8:9], v11, s11, v[12:13]
	v_or_b32_e32 v11, 2, v133
	v_sub_u32_e32 v13, 63, v11
	v_cndmask_b32_e64 v11, v13, v11, s[4:5]
	v_mad_u64_u32 v[32:33], s[8:9], v11, s11, v[12:13]
	v_or_b32_e32 v11, 3, v133
	v_sub_u32_e32 v13, 63, v11
	v_cndmask_b32_e64 v11, v13, v11, s[4:5]
	v_mad_u64_u32 v[12:13], s[8:9], v11, s11, v[12:13]
	v_add_u32_e32 v11, 0xffffff00, v0
	v_ashrrev_i32_e32 v11, 4, v11
	v_lshl_or_b32 v13, s10, 8, v177
	v_sub_u32_e32 v15, 63, v11
	v_or_b32_e32 v13, 0x2800, v13
	v_cndmask_b32_e64 v15, v15, v11, s[4:5]
	v_mad_i32_i24 v58, v15, s11, v13
	v_xor_b32_e32 v15, 63, v168
	v_cndmask_b32_e64 v15, v15, v168, s[4:5]
	v_mad_u32_u24 v60, v15, s11, v13
	v_add_u32_e32 v15, 0x100, v0
	v_lshrrev_b32_e32 v15, 4, v15
	v_xor_b32_e32 v17, 63, v15
	v_cndmask_b32_e64 v17, v17, v15, s[4:5]
	v_mad_i32_i24 v62, v17, s11, v13
	v_xor_b32_e32 v17, 63, v170
	v_cndmask_b32_e64 v17, v17, v170, s[4:5]
	v_add_u32_e32 v66, 0x800, v16
	v_add_u32_e32 v82, 0x800, v28
	v_add_u32_e32 v100, 0x800, v32
	v_add_u32_e32 v116, 0x800, v12
	v_mad_i32_i24 v64, v17, s11, v13
	v_add_u32_e32 v68, 0x2400, v16
	v_add_u32_e32 v70, 0x820, v16
	v_add_u32_e32 v72, 0x2420, v16
	v_add_u32_e32 v74, 0x840, v16
	v_add_u32_e32 v76, 0x2440, v16
	v_add_u32_e32 v78, 0x860, v16
	v_add_u32_e32 v80, 0x2460, v16
	v_add_u32_e32 v84, 0x2400, v28
	v_add_u32_e32 v88, 0x820, v28
	v_add_u32_e32 v90, 0x2420, v28
	v_add_u32_e32 v92, 0x840, v28
	v_add_u32_e32 v94, 0x2440, v28
	v_add_u32_e32 v96, 0x860, v28
	v_add_u32_e32 v98, 0x2460, v28
	v_add_u32_e32 v102, 0x2400, v32
	v_add_u32_e32 v104, 0x820, v32
	v_add_u32_e32 v106, 0x2420, v32
	v_add_u32_e32 v108, 0x840, v32
	v_add_u32_e32 v110, 0x2440, v32
	v_add_u32_e32 v112, 0x860, v32
	v_add_u32_e32 v114, 0x2460, v32
	v_add_u32_e32 v118, 0x2400, v12
	v_add_u32_e32 v120, 0x820, v12
	v_add_u32_e32 v122, 0x2420, v12
	v_add_u32_e32 v124, 0x840, v12
	v_add_u32_e32 v126, 0x2440, v12
	v_add_u32_e32 v128, 0x860, v12
	v_add_u32_e32 v130, 0x2460, v12
	global_load_ushort v35, v66, s[2:3]
	global_load_ushort v190, v68, s[2:3]
	global_load_ushort v214, v82, s[2:3]
	global_load_ushort v215, v84, s[2:3]
	global_load_ushort v222, v100, s[2:3]
	global_load_ushort v223, v102, s[2:3]
	global_load_ushort v231, v116, s[2:3]
	global_load_ushort v232, v118, s[2:3]
	global_load_ushort v191, v70, s[2:3]
	global_load_ushort v192, v72, s[2:3]
	global_load_ushort v216, v88, s[2:3]
	global_load_ushort v217, v90, s[2:3]
	global_load_ushort v224, v104, s[2:3]
	global_load_ushort v225, v106, s[2:3]
	global_load_ushort v233, v120, s[2:3]
	global_load_ushort v234, v122, s[2:3]
	global_load_ushort v193, v74, s[2:3]
	global_load_ushort v194, v76, s[2:3]
	global_load_ushort v218, v92, s[2:3]
	global_load_ushort v219, v94, s[2:3]
	global_load_ushort v226, v108, s[2:3]
	global_load_ushort v227, v110, s[2:3]
	global_load_ushort v235, v124, s[2:3]
	global_load_ushort v236, v126, s[2:3]
	global_load_ushort v195, v78, s[2:3]
	global_load_ushort v196, v80, s[2:3]
	global_load_ushort v220, v96, s[2:3]
	global_load_ushort v221, v98, s[2:3]
	global_load_ushort v229, v112, s[2:3]
	global_load_ushort v230, v114, s[2:3]
	global_load_ushort v237, v128, s[2:3]
	global_load_ushort v238, v130, s[2:3]
	global_load_dwordx4 v[40:43], v58, s[2:3]
	global_load_dwordx4 v[44:47], v60, s[2:3]
	global_load_dwordx4 v[48:51], v62, s[2:3]
	global_load_dwordx4 v[52:55], v64, s[2:3]
	v_lshlrev_b32_e32 v13, 2, v1
	s_add_i32 s13, 0, 0x11000
	v_add_u32_e32 v183, s13, v13
	s_add_i32 s13, 0, 0x11800
	v_add_u32_e32 v184, s13, v13
	s_add_i32 s13, 0, 0x22900
	v_add_u32_e32 v187, s13, v13
	s_add_i32 s13, 0, 0x23100
	v_add_u32_e32 v188, s13, v13
	s_add_i32 s13, 0, 0x19100
	s_lshl_b32 s36, s12, 8
	s_cmpk_gt_u32 s30, 0x13f
	s_movk_i32 s2, 0xa0
	s_cselect_b64 s[14:15], -1, 0
	s_cmpk_gt_u32 s30, 0x17f
	v_mul_lo_u32 v133, v133, s2
	s_cselect_b64 s[16:17], -1, 0
	s_cmpk_gt_u32 s30, 0x1bf
	v_add_u32_e32 v137, 0xa0, v133
	v_add_u32_e32 v138, 0x140, v133
	v_add_u32_e32 v139, 0x1e0, v133
	v_or_b32_e32 v134, 32, v132
	v_or_b32_e32 v135, 64, v132
	v_or_b32_e32 v136, 0x60, v132
	v_mul_i32_i24_e32 v185, 0x120, v11
	v_or_b32_e32 v11, s12, v86
	s_cselect_b64 s[18:19], -1, 0
	s_cmpk_gt_u32 s30, 0x1ff
	v_or_b32_e32 v197, v133, v132
	v_or_b32_e32 v198, v137, v132
	v_or_b32_e32 v199, v138, v132
	v_or_b32_e32 v200, v139, v132
	v_mbcnt_lo_u32_b32 v132, -1, 0
	v_mov_b32_e32 v59, v34
	v_mov_b32_e32 v61, v34
	v_mov_b32_e32 v63, v34
	v_mov_b32_e32 v65, v34
	v_cmp_lt_u32_e64 s[8:9], 1, v86
	v_cmp_eq_u32_e64 s[10:11], 3, v86
	v_mul_u32_u24_e32 v186, 0x120, v15
	v_add_u32_e32 v189, s13, v177
	v_mov_b32_e32 v67, v34
	v_mov_b32_e32 v69, v34
	v_mov_b32_e32 v71, v34
	v_mov_b32_e32 v73, v34
	v_mov_b32_e32 v75, v34
	v_mov_b32_e32 v77, v34
	v_mov_b32_e32 v79, v34
	v_mov_b32_e32 v81, v34
	v_mov_b32_e32 v83, v34
	v_mov_b32_e32 v85, v34
	v_mov_b32_e32 v89, v34
	v_mov_b32_e32 v91, v34
	v_mov_b32_e32 v93, v34
	v_mov_b32_e32 v95, v34
	v_mov_b32_e32 v97, v34
	v_mov_b32_e32 v99, v34
	v_mov_b32_e32 v101, v34
	v_mov_b32_e32 v103, v34
	v_mov_b32_e32 v105, v34
	v_mov_b32_e32 v107, v34
	v_mov_b32_e32 v109, v34
	v_mov_b32_e32 v111, v34
	v_mov_b32_e32 v113, v34
	v_mov_b32_e32 v115, v34
	v_mov_b32_e32 v117, v34
	v_mov_b32_e32 v119, v34
	v_mov_b32_e32 v121, v34
	v_mov_b32_e32 v123, v34
	v_mov_b32_e32 v125, v34
	v_mov_b32_e32 v127, v34
	v_mov_b32_e32 v129, v34
	v_mov_b32_e32 v131, v34
	v_cmp_eq_u32_e64 s[12:13], 0, v11
	s_waitcnt vmcnt(39)
	v_mov_b32_e32 v11, v10
	v_mov_b32_e32 v12, v10
	v_mov_b32_e32 v13, v10
	s_waitcnt vmcnt(38)
	v_mov_b32_e32 v15, v14
	v_mov_b32_e32 v16, v14
	v_mov_b32_e32 v17, v14
	s_waitcnt vmcnt(37)
	v_mov_b32_e32 v27, v26
	v_mov_b32_e32 v28, v26
	v_mov_b32_e32 v29, v26
	s_waitcnt vmcnt(36)
	v_mov_b32_e32 v31, v30
	v_mov_b32_e32 v32, v30
	v_mov_b32_e32 v33, v30
	s_cselect_b64 s[20:21], -1, 0
	v_or_b32_e32 v201, v133, v134
	v_add_u32_e32 v202, v137, v134
	v_or_b32_e32 v203, v138, v134
	v_add_u32_e32 v204, v139, v134
	v_or_b32_e32 v205, v133, v135
	v_or_b32_e32 v206, v137, v135
	v_add_u32_e32 v207, v138, v135
	v_add_u32_e32 v208, v139, v135
	v_or_b32_e32 v209, v133, v136
	v_add_u32_e32 v210, v137, v136
	v_add_u32_e32 v211, v138, v136
	v_add_u32_e32 v212, v139, v136
	s_movk_i32 s37, 0x1040
	s_movk_i32 s38, 0x80
	s_mov_b32 s39, -3
	s_mov_b32 s40, 0x3d800000
	s_add_i32 s41, 0, 0x11900
	s_add_i32 s42, 0, 0x14100
	s_add_i32 s43, 0, 0x16900
	v_mbcnt_hi_u32_b32 v213, -1, v132
	s_branch .LBB0_1145

.LBB0_1145:
	s_add_i32 s39, s39, 2
	s_cmpk_lt_i32 s39, 0x43
	s_cselect_b64 s[2:3], -1, 0
	s_cmpk_gt_i32 s39, 0x42
	s_waitcnt lgkmcnt(0)
	s_barrier
	s_cselect_b64 s[26:27], -1, 0
	s_and_b64 vcc, exec, s[26:27]
	s_cbranch_vccnz .LBB0_1155
	s_sub_i32 s66, s38, 64
	s_cmpk_gt_u32 s66, 0xff
	s_cbranch_scc0 .Lgla_c1_ctx
	s_add_i32 s67, s37, 64
	s_add_i32 s66, s38, 0xfffffec0
	s_and_b64 s[68:69], s[4:5], exec
	s_cselect_b32 s66, s66, s67
	s_add_i32 s66, s66, s24
	s_branch .Lgla_c1_mul
.Lgla_c1_ctx:
	s_add_i32 s67, s37, 0xfffff040
	s_and_b64 s[68:69], s[4:5], exec
	s_cselect_b32 s66, s66, s67
	s_add_i32 s66, s66, s35
.Lgla_c1_mul:
	s_mul_hi_i32 s65, s66, 0x3200
	s_mul_i32 s64, s66, 0x3200
	v_readlane_b32 s68, v254, 61
	v_readlane_b32 s69, v254, 62
	s_add_u32 s64, s68, s64
	s_addc_u32 s65, s69, s65
	s_and_saveexec_b64 s[68:69], s[6:7]
	global_load_dwordx4 v[250:253], v56, s[64:65]
	s_mov_b64 exec, s[68:69]
	s_waitcnt vmcnt(37)
	v_mfma_f32_16x16x32_bf16 v[152:155], v[36:39], v[6:9], v[10:13]
	v_add_u32_e32 v138, -16, v213
	v_and_b32_e32 v139, 64, v213
	v_cmp_lt_i32_e32 vcc, v138, v139
	v_add_u32_e32 v167, s36, v183
	s_nop 0
	v_cndmask_b32_e32 v138, v138, v213, vcc
	s_nop 1
	v_mul_f32_e32 v142, 0x3fb8aa3b, v152
	v_exp_f32_e64 v143, -|v142|
	v_mul_f32_e32 v146, 0x3fb8aa3b, v153
	v_exp_f32_e64 v147, -|v146|
	v_lshlrev_b32_e32 v164, 2, v138
	v_add_f32_e32 v138, 1.0, v143
	v_log_f32_e32 v138, v138
	v_add_f32_e32 v143, 1.0, v147
	v_log_f32_e32 v143, v143
	v_min_f32_e32 v142, 0, v142
	v_sub_f32_e32 v138, v142, v138
	v_min_f32_e32 v142, 0, v146
	v_fma_f32 v153, v138, s40, 0
	v_mul_f32_e32 v138, 0x3fb8aa3b, v154
	v_sub_f32_e32 v142, v142, v143
	v_exp_f32_e64 v143, -|v138|
	v_mul_f32_e32 v146, 0x3fb8aa3b, v155
	v_exp_f32_e64 v147, -|v146|
	v_fmamk_f32 v152, v142, 0x3d800000, v153
	v_add_f32_e32 v142, 1.0, v143
	v_log_f32_e32 v142, v142
	v_add_f32_e32 v143, 1.0, v147
	v_log_f32_e32 v143, v143
	v_min_f32_e32 v138, 0, v138
	v_sub_f32_e32 v138, v138, v142
	v_min_f32_e32 v142, 0, v146
	v_sub_f32_e32 v142, v142, v143
	v_fmamk_f32 v155, v138, 0x3d800000, v152
	v_fmamk_f32 v154, v142, 0x3d800000, v155
	v_subrev_u32_e32 v142, 32, v213
	v_cmp_lt_i32_e32 vcc, v142, v139
	v_cndmask_b32_e32 v139, v142, v213, vcc
	v_lshlrev_b32_e32 v239, 2, v139
	v_mfma_f32_16x16x32_bf16 v[160:163], v[36:39], v[2:5], v[14:17]
	s_nop 7
	v_mul_f32_e32 v138, 0x3fb8aa3b, v160
	v_exp_f32_e64 v142, -|v138|
	v_mul_f32_e32 v139, 0x3fb8aa3b, v161
	v_exp_f32_e64 v143, -|v139|
	v_min_f32_e32 v138, 0, v138
	v_add_f32_e32 v142, 1.0, v142
	v_log_f32_e32 v142, v142
	v_add_f32_e32 v143, 1.0, v143
	v_mul_f32_e32 v150, 0x3fb8aa3b, v162
	v_log_f32_e32 v143, v143
	v_sub_f32_e32 v138, v138, v142
	v_exp_f32_e64 v151, -|v150|
	v_fma_f32 v147, v138, s40, 0
	v_mul_f32_e32 v138, 0x3fb8aa3b, v163
	v_exp_f32_e64 v142, -|v138|
	v_min_f32_e32 v139, 0, v139
	v_sub_f32_e32 v139, v139, v143
	v_fmamk_f32 v146, v139, 0x3d800000, v147
	v_add_f32_e32 v139, 1.0, v151
	v_log_f32_e32 v139, v139
	v_add_f32_e32 v142, 1.0, v142
	v_log_f32_e32 v142, v142
	v_min_f32_e32 v143, 0, v150
	v_sub_f32_e32 v139, v143, v139
	v_min_f32_e32 v138, 0, v138
	v_sub_f32_e32 v138, v138, v142
	v_fmamk_f32 v151, v139, 0x3d800000, v146
	v_fmamk_f32 v150, v138, 0x3d800000, v151
	v_mfma_f32_16x16x32_bf16 v[160:163], v[36:39], v[22:25], v[26:29]
	s_nop 7
	v_mul_f32_e32 v138, 0x3fb8aa3b, v160
	v_mul_f32_e32 v139, 0x3fb8aa3b, v161
	v_exp_f32_e64 v142, -|v138|
	v_exp_f32_e64 v143, -|v139|
	v_mul_f32_e32 v160, 0x3fb8aa3b, v162
	v_min_f32_e32 v138, 0, v138
	v_add_f32_e32 v142, 1.0, v142
	v_add_f32_e32 v143, 1.0, v143
	v_log_f32_e32 v142, v142
	v_log_f32_e32 v143, v143
	v_min_f32_e32 v139, 0, v139
	v_exp_f32_e64 v161, -|v160|
	v_sub_f32_e32 v138, v138, v142
	v_sub_f32_e32 v142, v139, v143
	v_mul_f32_e32 v143, 0x3fb8aa3b, v163
	v_exp_f32_e64 v162, -|v143|
	v_fma_f32 v139, v138, s40, 0
	v_fmamk_f32 v138, v142, 0x3d800000, v139
	v_add_f32_e32 v142, 1.0, v161
	v_log_f32_e32 v142, v142
	v_add_f32_e32 v161, 1.0, v162
	v_log_f32_e32 v161, v161
	v_min_f32_e32 v160, 0, v160
	v_sub_f32_e32 v142, v160, v142
	v_min_f32_e32 v143, 0, v143
	v_sub_f32_e32 v160, v143, v161
	v_fmamk_f32 v143, v142, 0x3d800000, v138
	v_fmamk_f32 v142, v160, 0x3d800000, v143
	v_mfma_f32_16x16x32_bf16 v[160:163], v[36:39], v[18:21], v[30:33]
	s_nop 7
	v_mul_f32_e32 v160, 0x3fb8aa3b, v160
	v_mul_f32_e32 v161, 0x3fb8aa3b, v161
	v_exp_f32_e64 v244, -|v160|
	v_exp_f32_e64 v245, -|v161|
	v_mul_f32_e32 v162, 0x3fb8aa3b, v162
	v_min_f32_e32 v160, 0, v160
	v_add_f32_e32 v244, 1.0, v244
	v_add_f32_e32 v245, 1.0, v245
	v_log_f32_e32 v244, v244
	v_log_f32_e32 v245, v245
	v_min_f32_e32 v161, 0, v161
	v_exp_f32_e64 v246, -|v162|
	v_mul_f32_e32 v163, 0x3fb8aa3b, v163
	v_sub_f32_e32 v160, v160, v244
	v_sub_f32_e32 v244, v161, v245
	v_exp_f32_e64 v245, -|v163|
	v_fma_f32 v161, v160, s40, 0
	v_fmamk_f32 v160, v244, 0x3d800000, v161
	v_add_f32_e32 v244, 1.0, v246
	v_log_f32_e32 v244, v244
	v_add_f32_e32 v245, 1.0, v245
	v_log_f32_e32 v245, v245
	v_min_f32_e32 v162, 0, v162
	v_sub_f32_e32 v162, v162, v244
	v_min_f32_e32 v163, 0, v163
	v_sub_f32_e32 v244, v163, v245
	v_fmamk_f32 v163, v162, 0x3d800000, v160
	v_fmamk_f32 v162, v244, 0x3d800000, v163
	ds_bpermute_b32 v247, v164, v154
	ds_bpermute_b32 v248, v164, v150
	ds_bpermute_b32 v249, v164, v142
	ds_bpermute_b32 v131, v164, v162
	s_waitcnt lgkmcnt(0)
	v_add_f32_e32 v247, v154, v247
	v_add_f32_e32 v248, v150, v248
	v_add_f32_e32 v249, v142, v249
	v_add_f32_e32 v131, v162, v131
	v_cndmask_b32_e64 v165, v247, v154, s[0:1]
	v_cndmask_b32_e64 v240, v248, v150, s[0:1]
	v_cndmask_b32_e64 v242, v249, v142, s[0:1]
	v_cndmask_b32_e64 v164, v131, v162, s[0:1]
	ds_bpermute_b32 v247, v239, v165
	ds_bpermute_b32 v248, v239, v240
	ds_bpermute_b32 v249, v239, v242
	ds_bpermute_b32 v131, v239, v164
	s_waitcnt lgkmcnt(0)
	v_add_f32_e32 v166, v165, v247
	v_add_f32_e32 v241, v240, v248
	v_add_f32_e32 v243, v242, v249
	v_add_f32_e32 v239, v164, v131
	s_and_saveexec_b64 s[28:29], s[10:11]
	ds_write_b32 v167, v166
	ds_write_b32 v167, v241 offset:64
	ds_write_b32 v167, v243 offset:128
	ds_write_b32 v167, v239 offset:192
	s_or_b64 exec, exec, s[28:29]
	v_cndmask_b32_e64 v167, v242, v243, s[8:9]
	v_sub_f32_e32 v242, v167, v142
	v_cndmask_b32_e64 v167, v240, v241, s[8:9]
	v_cndmask_b32_e64 v165, v165, v166, s[8:9]
	v_cndmask_b32_e64 v164, v164, v239, s[8:9]
	v_sub_f32_e32 v240, v167, v150
	v_sub_f32_e32 v166, v165, v154
	v_sub_f32_e32 v164, v164, v162
	v_pk_add_f32 v[138:139], v[138:139], v[242:243] op_sel_hi:[1,0]
	v_pk_add_f32 v[142:143], v[142:143], v[242:243] op_sel_hi:[1,0]
	v_pk_add_f32 v[146:147], v[146:147], v[240:241] op_sel_hi:[1,0]
	v_pk_add_f32 v[150:151], v[150:151], v[240:241] op_sel_hi:[1,0]
	v_pk_add_f32 v[152:153], v[152:153], v[166:167] op_sel_hi:[1,0]
	v_pk_add_f32 v[154:155], v[154:155], v[166:167] op_sel_hi:[1,0]
	v_pk_add_f32 v[160:161], v[160:161], v[164:165] op_sel_hi:[1,0]
	v_pk_add_f32 v[162:163], v[162:163], v[164:165] op_sel_hi:[1,0]
.LBB0_1155:
	s_waitcnt lgkmcnt(0)
	s_barrier
	s_andn2_b64 vcc, exec, s[2:3]
	s_cbranch_vccnz .LBB0_1172
	ds_read2st64_b32 v[166:167], v183 offset1:1
	ds_read2st64_b32 v[164:165], v183 offset0:2 offset1:3
	s_waitcnt lgkmcnt(1)
	v_add_f32_e32 v166, 0, v166
	v_add_f32_e32 v239, v166, v167
	s_waitcnt lgkmcnt(0)
	v_add_f32_e32 v239, v239, v164
	v_add_f32_e32 v239, v239, v165
	v_exp_f32_e32 v243, v239
	s_and_saveexec_b64 s[2:3], s[12:13]
	ds_write_b32 v184, v243
	s_or_b64 exec, exec, s[2:3]
	v_cndmask_b32_e64 v166, 0, v166, s[14:15]
	v_cndmask_b32_e64 v167, 0, v167, s[16:17]
	v_add_f32_e32 v166, v166, v167
	v_cndmask_b32_e64 v164, 0, v164, s[18:19]
	v_add_f32_e32 v164, v166, v164
	v_cndmask_b32_e64 v165, 0, v165, s[20:21]
	v_add_f32_e32 v164, v164, v165
	v_add_f32_e32 v165, v153, v164
	v_exp_f32_e64 v167, -v165
	v_exp_f32_e32 v165, v165
	s_waitcnt vmcnt(36)
	v_lshlrev_b32_e32 v166, 16, v35
	v_mul_f32_e32 v166, 0x3e000000, v166
	s_waitcnt vmcnt(35)
	v_lshlrev_b32_e32 v239, 16, v190
	v_mul_f32_e32 v165, v166, v165
	v_mul_f32_e32 v167, v167, v239
	v_cvt_pk_bf16_f32 v165, v165, s0
	v_add_u32_e32 v239, 0, v197
	ds_write_b16 v239, v165
	v_cvt_pk_bf16_f32 v165, v167, s0
	ds_write_b16 v239, v165 offset:10240
	v_mul_f32_e32 v165, v243, v167
	v_cvt_pk_bf16_f32 v165, v165, s0
	ds_write_b16 v239, v165 offset:20480
	v_add_f32_e32 v165, v152, v164
	v_exp_f32_e64 v167, -v165
	v_exp_f32_e32 v165, v165
	s_waitcnt vmcnt(34)
	v_lshlrev_b32_e32 v166, 16, v214
	v_mul_f32_e32 v166, 0x3e000000, v166
	s_waitcnt vmcnt(33)
	v_lshlrev_b32_e32 v240, 16, v215
	v_mul_f32_e32 v165, v166, v165
	v_mul_f32_e32 v167, v167, v240
	v_cvt_pk_bf16_f32 v165, v165, s0
	v_add_u32_e32 v240, 0, v198
	ds_write_b16 v240, v165
	v_cvt_pk_bf16_f32 v165, v167, s0
	ds_write_b16 v240, v165 offset:10240
	v_mul_f32_e32 v165, v243, v167
	v_cvt_pk_bf16_f32 v165, v165, s0
	ds_write_b16 v240, v165 offset:20480
	v_add_f32_e32 v165, v155, v164
	v_exp_f32_e64 v167, -v165
	v_exp_f32_e32 v165, v165
	s_waitcnt vmcnt(32)
	v_lshlrev_b32_e32 v166, 16, v222
	v_mul_f32_e32 v166, 0x3e000000, v166
	s_waitcnt vmcnt(31)
	v_lshlrev_b32_e32 v241, 16, v223
	v_mul_f32_e32 v165, v166, v165
	v_mul_f32_e32 v167, v167, v241
	v_cvt_pk_bf16_f32 v165, v165, s0
	v_add_u32_e32 v241, 0, v199
	ds_write_b16 v241, v165
	v_cvt_pk_bf16_f32 v165, v167, s0
	v_add_f32_e32 v164, v154, v164
	ds_write_b16 v241, v165 offset:10240
	v_mul_f32_e32 v165, v243, v167
	v_exp_f32_e64 v166, -v164
	v_exp_f32_e32 v164, v164
	v_cvt_pk_bf16_f32 v165, v165, s0
	ds_write_b16 v241, v165 offset:20480
	s_waitcnt vmcnt(30)
	v_lshlrev_b32_e32 v165, 16, v231
	v_mul_f32_e32 v165, 0x3e000000, v165
	s_waitcnt vmcnt(29)
	v_lshlrev_b32_e32 v167, 16, v232
	global_load_ushort v35, v66, s[64:65]
	global_load_ushort v190, v68, s[64:65]
	global_load_ushort v214, v82, s[64:65]
	global_load_ushort v215, v84, s[64:65]
	global_load_ushort v222, v100, s[64:65]
	global_load_ushort v223, v102, s[64:65]
	global_load_ushort v231, v116, s[64:65]
	global_load_ushort v232, v118, s[64:65]
	v_mul_f32_e32 v164, v165, v164
	v_mul_f32_e32 v245, v166, v167
	v_cvt_pk_bf16_f32 v166, v164, s0
	ds_read2_b32 v[164:165], v183 offset0:16 offset1:80
	v_add_u32_e32 v242, 0, v200
	ds_write_b16 v242, v166
	ds_read2_b32 v[166:167], v183 offset0:144 offset1:208
	v_cvt_pk_bf16_f32 v244, v245, s0
	s_waitcnt lgkmcnt(2)
	v_add_f32_e32 v164, 0, v164
	ds_write_b16 v242, v244 offset:10240
	v_add_f32_e32 v244, v164, v165
	s_waitcnt lgkmcnt(1)
	v_add_f32_e32 v244, v244, v166
	v_add_f32_e32 v244, v244, v167
	v_exp_f32_e32 v244, v244
	v_mul_f32_e32 v243, v243, v245
	v_cvt_pk_bf16_f32 v243, v243, s0
	ds_write_b16 v242, v243 offset:20480
	s_and_saveexec_b64 s[2:3], s[12:13]
	ds_write_b32 v184, v244 offset:64
	s_or_b64 exec, exec, s[2:3]
	v_cndmask_b32_e64 v164, 0, v164, s[14:15]
	v_cndmask_b32_e64 v165, 0, v165, s[16:17]
	v_add_f32_e32 v164, v164, v165
	v_cndmask_b32_e64 v165, 0, v166, s[18:19]
	v_add_f32_e32 v164, v164, v165
	v_cndmask_b32_e64 v165, 0, v167, s[20:21]
	v_add_f32_e32 v164, v164, v165
	v_add_f32_e32 v165, v147, v164
	v_exp_f32_e64 v167, -v165
	v_exp_f32_e32 v165, v165
	s_waitcnt vmcnt(36)
	v_lshlrev_b32_e32 v166, 16, v191
	v_mul_f32_e32 v166, 0x3e000000, v166
	s_waitcnt vmcnt(35)
	v_lshlrev_b32_e32 v243, 16, v192
	v_mul_f32_e32 v165, v166, v165
	v_mul_f32_e32 v167, v167, v243
	v_cvt_pk_bf16_f32 v165, v165, s0
	ds_write_b16 v239, v165 offset:32
	v_cvt_pk_bf16_f32 v165, v167, s0
	ds_write_b16 v239, v165 offset:10272
	v_mul_f32_e32 v165, v244, v167
	v_cvt_pk_bf16_f32 v165, v165, s0
	ds_write_b16 v239, v165 offset:20512
	v_add_f32_e32 v165, v146, v164
	v_exp_f32_e64 v167, -v165
	v_exp_f32_e32 v165, v165
	s_waitcnt vmcnt(34)
	v_lshlrev_b32_e32 v166, 16, v216
	v_mul_f32_e32 v166, 0x3e000000, v166
	s_waitcnt vmcnt(33)
	v_lshlrev_b32_e32 v243, 16, v217
	v_mul_f32_e32 v165, v166, v165
	v_mul_f32_e32 v167, v167, v243
	v_cvt_pk_bf16_f32 v165, v165, s0
	ds_write_b16 v240, v165 offset:32
	v_cvt_pk_bf16_f32 v165, v167, s0
	ds_write_b16 v240, v165 offset:10272
	v_mul_f32_e32 v165, v244, v167
	v_cvt_pk_bf16_f32 v165, v165, s0
	ds_write_b16 v240, v165 offset:20512
	v_add_f32_e32 v165, v151, v164
	v_exp_f32_e64 v167, -v165
	v_exp_f32_e32 v165, v165
	s_waitcnt vmcnt(32)
	v_lshlrev_b32_e32 v166, 16, v224
	v_mul_f32_e32 v166, 0x3e000000, v166
	s_waitcnt vmcnt(31)
	v_lshlrev_b32_e32 v243, 16, v225
	v_mul_f32_e32 v165, v166, v165
	v_mul_f32_e32 v167, v167, v243
	v_cvt_pk_bf16_f32 v165, v165, s0
	ds_write_b16 v241, v165 offset:32
	v_cvt_pk_bf16_f32 v165, v167, s0
	v_add_f32_e32 v164, v150, v164
	ds_write_b16 v241, v165 offset:10272
	v_mul_f32_e32 v165, v244, v167
	v_exp_f32_e64 v166, -v164
	v_exp_f32_e32 v164, v164
	v_cvt_pk_bf16_f32 v165, v165, s0
	ds_write_b16 v241, v165 offset:20512
	s_waitcnt vmcnt(30)
	v_lshlrev_b32_e32 v165, 16, v233
	v_mul_f32_e32 v165, 0x3e000000, v165
	s_waitcnt vmcnt(29)
	v_lshlrev_b32_e32 v167, 16, v234
	global_load_ushort v191, v70, s[64:65]
	global_load_ushort v192, v72, s[64:65]
	global_load_ushort v216, v88, s[64:65]
	global_load_ushort v217, v90, s[64:65]
	global_load_ushort v224, v104, s[64:65]
	global_load_ushort v225, v106, s[64:65]
	global_load_ushort v233, v120, s[64:65]
	global_load_ushort v234, v122, s[64:65]
	v_mul_f32_e32 v164, v165, v164
	v_mul_f32_e32 v245, v166, v167
	v_cvt_pk_bf16_f32 v166, v164, s0
	ds_read2_b32 v[164:165], v183 offset0:32 offset1:96
	ds_write_b16 v242, v166 offset:32
	ds_read2_b32 v[166:167], v183 offset0:160 offset1:224
	v_cvt_pk_bf16_f32 v243, v245, s0
	ds_write_b16 v242, v243 offset:10272
	s_waitcnt lgkmcnt(3)
	v_add_f32_e32 v164, 0, v164
	v_add_f32_e32 v243, v164, v165
	s_waitcnt lgkmcnt(1)
	v_add_f32_e32 v243, v243, v166
	v_add_f32_e32 v243, v243, v167
	v_exp_f32_e32 v243, v243
	v_mul_f32_e32 v244, v244, v245
	v_cvt_pk_bf16_f32 v244, v244, s0
	ds_write_b16 v242, v244 offset:20512
	s_and_saveexec_b64 s[2:3], s[12:13]
	ds_write_b32 v184, v243 offset:128
	s_or_b64 exec, exec, s[2:3]
	v_cndmask_b32_e64 v164, 0, v164, s[14:15]
	v_cndmask_b32_e64 v165, 0, v165, s[16:17]
	v_add_f32_e32 v164, v164, v165
	v_cndmask_b32_e64 v165, 0, v166, s[18:19]
	v_add_f32_e32 v164, v164, v165
	v_cndmask_b32_e64 v165, 0, v167, s[20:21]
	v_add_f32_e32 v164, v164, v165
	v_add_f32_e32 v165, v139, v164
	v_exp_f32_e64 v167, -v165
	v_exp_f32_e32 v165, v165
	s_waitcnt vmcnt(36)
	v_lshlrev_b32_e32 v166, 16, v193
	v_mul_f32_e32 v166, 0x3e000000, v166
	s_waitcnt vmcnt(35)
	v_lshlrev_b32_e32 v244, 16, v194
	v_mul_f32_e32 v165, v166, v165
	v_mul_f32_e32 v167, v167, v244
	v_cvt_pk_bf16_f32 v165, v165, s0
	ds_write_b16 v239, v165 offset:64
	v_cvt_pk_bf16_f32 v165, v167, s0
	ds_write_b16 v239, v165 offset:10304
	v_mul_f32_e32 v165, v243, v167
	v_cvt_pk_bf16_f32 v165, v165, s0
	ds_write_b16 v239, v165 offset:20544
	v_add_f32_e32 v165, v138, v164
	v_exp_f32_e64 v167, -v165
	v_exp_f32_e32 v165, v165
	s_waitcnt vmcnt(34)
	v_lshlrev_b32_e32 v166, 16, v218
	v_mul_f32_e32 v166, 0x3e000000, v166
	s_waitcnt vmcnt(33)
	v_lshlrev_b32_e32 v244, 16, v219
	v_mul_f32_e32 v165, v166, v165
	v_mul_f32_e32 v167, v167, v244
	v_cvt_pk_bf16_f32 v165, v165, s0
	ds_write_b16 v240, v165 offset:64
	v_cvt_pk_bf16_f32 v165, v167, s0
	ds_write_b16 v240, v165 offset:10304
	v_mul_f32_e32 v165, v243, v167
	v_cvt_pk_bf16_f32 v165, v165, s0
	ds_write_b16 v240, v165 offset:20544
	v_add_f32_e32 v165, v143, v164
	v_exp_f32_e64 v167, -v165
	v_exp_f32_e32 v165, v165
	s_waitcnt vmcnt(32)
	v_lshlrev_b32_e32 v166, 16, v226
	v_mul_f32_e32 v166, 0x3e000000, v166
	s_waitcnt vmcnt(31)
	v_lshlrev_b32_e32 v244, 16, v227
	v_mul_f32_e32 v165, v166, v165
	v_mul_f32_e32 v167, v167, v244
	v_cvt_pk_bf16_f32 v165, v165, s0
	ds_write_b16 v241, v165 offset:64
	v_cvt_pk_bf16_f32 v165, v167, s0
	v_add_f32_e32 v164, v142, v164
	ds_write_b16 v241, v165 offset:10304
	v_mul_f32_e32 v165, v243, v167
	v_exp_f32_e64 v166, -v164
	v_exp_f32_e32 v164, v164
	v_cvt_pk_bf16_f32 v165, v165, s0
	ds_write_b16 v241, v165 offset:20544
	s_waitcnt vmcnt(30)
	v_lshlrev_b32_e32 v165, 16, v235
	v_mul_f32_e32 v165, 0x3e000000, v165
	s_waitcnt vmcnt(29)
	v_lshlrev_b32_e32 v167, 16, v236
	global_load_ushort v193, v74, s[64:65]
	global_load_ushort v194, v76, s[64:65]
	global_load_ushort v218, v92, s[64:65]
	global_load_ushort v219, v94, s[64:65]
	global_load_ushort v226, v108, s[64:65]
	global_load_ushort v227, v110, s[64:65]
	global_load_ushort v235, v124, s[64:65]
	global_load_ushort v236, v126, s[64:65]
	v_mul_f32_e32 v164, v165, v164
	v_mul_f32_e32 v245, v166, v167
	v_cvt_pk_bf16_f32 v166, v164, s0
	ds_read2_b32 v[164:165], v183 offset0:48 offset1:112
	ds_write_b16 v242, v166 offset:64
	ds_read2_b32 v[166:167], v183 offset0:176 offset1:240
	v_cvt_pk_bf16_f32 v244, v245, s0
	ds_write_b16 v242, v244 offset:10304
	s_waitcnt lgkmcnt(3)
	v_add_f32_e32 v244, 0, v164
	v_add_f32_e32 v164, v244, v165
	s_waitcnt lgkmcnt(1)
	v_add_f32_e32 v164, v164, v166
	v_add_f32_e32 v164, v164, v167
	v_exp_f32_e32 v164, v164
	v_mul_f32_e32 v243, v243, v245
	v_cvt_pk_bf16_f32 v243, v243, s0
	ds_write_b16 v242, v243 offset:20544
	s_and_saveexec_b64 s[2:3], s[12:13]
	ds_write_b32 v184, v164 offset:192
	s_or_b64 exec, exec, s[2:3]
	v_cndmask_b32_e64 v243, 0, v244, s[14:15]
	v_cndmask_b32_e64 v165, 0, v165, s[16:17]
	v_add_f32_e32 v165, v243, v165
	v_cndmask_b32_e64 v166, 0, v166, s[18:19]
	v_add_f32_e32 v165, v165, v166
	v_cndmask_b32_e64 v166, 0, v167, s[20:21]
	v_add_f32_e32 v165, v165, v166
	v_add_f32_e32 v166, v161, v165
	v_exp_f32_e64 v243, -v166
	v_exp_f32_e32 v166, v166
	s_waitcnt vmcnt(36)
	v_lshlrev_b32_e32 v167, 16, v195
	v_mul_f32_e32 v167, 0x3e000000, v167
	s_waitcnt vmcnt(35)
	v_lshlrev_b32_e32 v244, 16, v196
	v_mul_f32_e32 v166, v167, v166
	v_mul_f32_e32 v243, v243, v244
	v_cvt_pk_bf16_f32 v166, v166, s0
	ds_write_b16 v239, v166 offset:96
	v_cvt_pk_bf16_f32 v166, v243, s0
	ds_write_b16 v239, v166 offset:10336
	v_mul_f32_e32 v166, v164, v243
	v_cvt_pk_bf16_f32 v166, v166, s0
	ds_write_b16 v239, v166 offset:20576
	v_add_f32_e32 v166, v160, v165
	v_exp_f32_e64 v239, -v166
	v_exp_f32_e32 v166, v166
	s_waitcnt vmcnt(34)
	v_lshlrev_b32_e32 v167, 16, v220
	v_mul_f32_e32 v167, 0x3e000000, v167
	s_waitcnt vmcnt(33)
	v_lshlrev_b32_e32 v243, 16, v221
	v_mul_f32_e32 v166, v167, v166
	v_mul_f32_e32 v239, v239, v243
	v_cvt_pk_bf16_f32 v166, v166, s0
	ds_write_b16 v240, v166 offset:96
	v_cvt_pk_bf16_f32 v166, v239, s0
	ds_write_b16 v240, v166 offset:10336
	v_mul_f32_e32 v166, v164, v239
	v_cvt_pk_bf16_f32 v166, v166, s0
	ds_write_b16 v240, v166 offset:20576
	v_add_f32_e32 v166, v163, v165
	v_exp_f32_e64 v239, -v166
	v_exp_f32_e32 v166, v166
	s_waitcnt vmcnt(32)
	v_lshlrev_b32_e32 v167, 16, v229
	v_mul_f32_e32 v167, 0x3e000000, v167
	s_waitcnt vmcnt(31)
	v_lshlrev_b32_e32 v240, 16, v230
	v_mul_f32_e32 v166, v167, v166
	v_mul_f32_e32 v239, v239, v240
	v_cvt_pk_bf16_f32 v166, v166, s0
	v_add_f32_e32 v165, v162, v165
	ds_write_b16 v241, v166 offset:96
	v_cvt_pk_bf16_f32 v166, v239, s0
	v_exp_f32_e64 v167, -v165
	ds_write_b16 v241, v166 offset:10336
	v_mul_f32_e32 v166, v164, v239
	v_exp_f32_e32 v165, v165
	v_cvt_pk_bf16_f32 v166, v166, s0
	ds_write_b16 v241, v166 offset:20576
	s_waitcnt vmcnt(30)
	v_lshlrev_b32_e32 v166, 16, v237
	s_waitcnt vmcnt(29)
	v_lshlrev_b32_e32 v239, 16, v238
	global_load_ushort v195, v78, s[64:65]
	global_load_ushort v196, v80, s[64:65]
	global_load_ushort v220, v96, s[64:65]
	global_load_ushort v221, v98, s[64:65]
	global_load_ushort v229, v112, s[64:65]
	global_load_ushort v230, v114, s[64:65]
	global_load_ushort v237, v128, s[64:65]
	global_load_ushort v238, v130, s[64:65]
	v_mul_f32_e32 v166, 0x3e000000, v166
	v_mul_f32_e32 v167, v167, v239
	v_mul_f32_e32 v165, v166, v165
	v_mul_f32_e32 v164, v164, v167
	v_cvt_pk_bf16_f32 v165, v165, s0
	v_cvt_pk_bf16_f32 v164, v164, s0
	ds_write_b16 v242, v165 offset:96
	v_cvt_pk_bf16_f32 v165, v167, s0
	ds_write_b16 v242, v164 offset:20576
	v_add_u32_e32 v164, v174, v185
	ds_write_b16 v242, v165 offset:10336
	s_waitcnt vmcnt(36)
	ds_write_b128 v164, v[40:43] offset:30720
	v_add_u32_e32 v164, v174, v171
	s_waitcnt vmcnt(35)
	ds_write_b128 v164, v[44:47] offset:30720
	v_add_u32_e32 v164, v174, v186
	s_waitcnt vmcnt(34)
	ds_write_b128 v164, v[48:51] offset:30720
	v_add_u32_e32 v164, v174, v172
	s_waitcnt vmcnt(33)
	ds_write_b128 v164, v[52:55] offset:30720
	global_load_dwordx4 v[40:43], v58, s[64:65]
	global_load_dwordx4 v[44:47], v60, s[64:65]
	global_load_dwordx4 v[48:51], v62, s[64:65]
	global_load_dwordx4 v[52:55], v64, s[64:65]
.LBB0_1172:
	s_waitcnt lgkmcnt(0)
	s_barrier
	s_cmpk_lt_i32 s39, 0x42
	s_cselect_b64 s[2:3], -1, 0
	s_cmpk_gt_i32 s39, 0x41
	s_cbranch_scc1 .LBB0_1182
	s_cmpk_eq_i32 s37, 0xffc0
	s_cbranch_scc1 .Lgla_c2_done
	s_cmpk_gt_u32 s38, 0xff
	s_cbranch_scc0 .Lgla_c2_ctx
	s_add_i32 s66, s38, 0xffffff00
	s_and_b64 s[68:69], s[4:5], exec
	s_cselect_b32 s66, s66, s37
	s_add_i32 s66, s66, s24
	s_branch .Lgla_c2_mul
.Lgla_c2_ctx:
	s_add_i32 s66, s37, 0xfffff000
	s_and_b64 s[68:69], s[4:5], exec
	s_cselect_b32 s66, s38, s66
	s_add_i32 s66, s66, s35
.Lgla_c2_mul:
	s_mul_hi_i32 s65, s66, 0x3200
	s_mul_i32 s64, s66, 0x3200
	v_readlane_b32 s68, v254, 61
	v_readlane_b32 s69, v254, 62
	s_add_u32 s64, s68, s64
	s_addc_u32 s65, s69, s65
.Lgla_c2_done:
	s_and_saveexec_b64 s[68:69], s[6:7]
	global_load_dwordx4 v[36:39], v56, s[64:65]
	s_mov_b64 exec, s[68:69]
	v_add_u32_e32 v132, -16, v213
	v_and_b32_e32 v136, 64, v213
	v_cmp_lt_i32_e32 vcc, v132, v136
	v_add_u32_e32 v167, s36, v187
	s_nop 0
	v_cndmask_b32_e32 v137, v132, v213, vcc
	s_waitcnt vmcnt(37)
	v_mfma_f32_16x16x32_bf16 v[132:135], v[250:253], v[6:9], v[10:13]
	v_lshlrev_b32_e32 v164, 2, v137
	s_nop 6
	v_mul_f32_e32 v132, 0x3fb8aa3b, v132
	v_exp_f32_e64 v140, -|v132|
	v_mul_f32_e32 v133, 0x3fb8aa3b, v133
	v_exp_f32_e64 v141, -|v133|
	v_min_f32_e32 v132, 0, v132
	v_add_f32_e32 v137, 1.0, v140
	v_log_f32_e32 v137, v137
	v_add_f32_e32 v140, 1.0, v141
	v_log_f32_e32 v140, v140
	v_mul_f32_e32 v135, 0x3fb8aa3b, v135
	v_sub_f32_e32 v132, v132, v137
	v_fma_f32 v145, v132, s40, 0
	v_mul_f32_e32 v132, 0x3fb8aa3b, v134
	v_exp_f32_e64 v134, -|v132|
	v_exp_f32_e64 v137, -|v135|
	v_min_f32_e32 v133, 0, v133
	v_sub_f32_e32 v133, v133, v140
	v_fmamk_f32 v144, v133, 0x3d800000, v145
	v_add_f32_e32 v133, 1.0, v134
	v_log_f32_e32 v133, v133
	v_add_f32_e32 v134, 1.0, v137
	v_log_f32_e32 v134, v134
	v_min_f32_e32 v132, 0, v132
	v_sub_f32_e32 v132, v132, v133
	v_min_f32_e32 v133, 0, v135
	v_sub_f32_e32 v133, v133, v134
	v_fmamk_f32 v149, v132, 0x3d800000, v144
	v_fmamk_f32 v148, v133, 0x3d800000, v149
	v_subrev_u32_e32 v133, 32, v213
	v_cmp_lt_i32_e32 vcc, v133, v136
	v_cndmask_b32_e32 v133, v133, v213, vcc
	v_lshlrev_b32_e32 v239, 2, v133
	v_mfma_f32_16x16x32_bf16 v[132:135], v[250:253], v[2:5], v[14:17]
	s_nop 7
	v_mul_f32_e32 v132, 0x3fb8aa3b, v132
	v_mul_f32_e32 v133, 0x3fb8aa3b, v133
	v_exp_f32_e64 v136, -|v132|
	v_exp_f32_e64 v137, -|v133|
	v_min_f32_e32 v132, 0, v132
	v_mul_f32_e32 v134, 0x3fb8aa3b, v134
	v_add_f32_e32 v136, 1.0, v136
	v_add_f32_e32 v137, 1.0, v137
	v_log_f32_e32 v136, v136
	v_log_f32_e32 v137, v137
	v_min_f32_e32 v133, 0, v133
	v_exp_f32_e64 v140, -|v134|
	v_sub_f32_e32 v132, v132, v136
	v_sub_f32_e32 v133, v133, v137
	v_fma_f32 v137, v132, s40, 0
	v_mul_f32_e32 v132, 0x3fb8aa3b, v135
	v_exp_f32_e64 v135, -|v132|
	v_fmamk_f32 v136, v133, 0x3d800000, v137
	v_add_f32_e32 v133, 1.0, v140
	v_log_f32_e32 v133, v133
	v_add_f32_e32 v135, 1.0, v135
	v_log_f32_e32 v135, v135
	v_min_f32_e32 v134, 0, v134
	v_sub_f32_e32 v133, v134, v133
	v_min_f32_e32 v132, 0, v132
	v_sub_f32_e32 v132, v132, v135
	v_fmamk_f32 v141, v133, 0x3d800000, v136
	v_fmamk_f32 v140, v132, 0x3d800000, v141
	v_mfma_f32_16x16x32_bf16 v[132:135], v[250:253], v[22:25], v[26:29]
	s_nop 7
	v_mul_f32_e32 v132, 0x3fb8aa3b, v132
	v_mul_f32_e32 v133, 0x3fb8aa3b, v133
	v_exp_f32_e64 v156, -|v132|
	v_exp_f32_e64 v157, -|v133|
	v_mul_f32_e32 v134, 0x3fb8aa3b, v134
	v_min_f32_e32 v132, 0, v132
	v_add_f32_e32 v156, 1.0, v156
	v_add_f32_e32 v157, 1.0, v157
	v_log_f32_e32 v156, v156
	v_log_f32_e32 v157, v157
	v_min_f32_e32 v133, 0, v133
	v_exp_f32_e64 v158, -|v134|
	v_mul_f32_e32 v135, 0x3fb8aa3b, v135
	v_sub_f32_e32 v132, v132, v156
	v_sub_f32_e32 v156, v133, v157
	v_exp_f32_e64 v157, -|v135|
	v_fma_f32 v133, v132, s40, 0
	v_fmamk_f32 v132, v156, 0x3d800000, v133
	v_add_f32_e32 v156, 1.0, v158
	v_log_f32_e32 v156, v156
	v_add_f32_e32 v157, 1.0, v157
	v_log_f32_e32 v157, v157
	v_min_f32_e32 v134, 0, v134
	v_sub_f32_e32 v134, v134, v156
	v_min_f32_e32 v135, 0, v135
	v_sub_f32_e32 v156, v135, v157
	v_fmamk_f32 v135, v134, 0x3d800000, v132
	v_fmamk_f32 v134, v156, 0x3d800000, v135
	v_mfma_f32_16x16x32_bf16 v[156:159], v[250:253], v[18:21], v[30:33]
	s_nop 7
	v_mul_f32_e32 v156, 0x3fb8aa3b, v156
	v_mul_f32_e32 v157, 0x3fb8aa3b, v157
	v_exp_f32_e64 v244, -|v156|
	v_exp_f32_e64 v245, -|v157|
	v_mul_f32_e32 v158, 0x3fb8aa3b, v158
	v_min_f32_e32 v156, 0, v156
	v_add_f32_e32 v244, 1.0, v244
	v_add_f32_e32 v245, 1.0, v245
	v_log_f32_e32 v244, v244
	v_log_f32_e32 v245, v245
	v_min_f32_e32 v157, 0, v157
	v_exp_f32_e64 v246, -|v158|
	v_mul_f32_e32 v159, 0x3fb8aa3b, v159
	v_sub_f32_e32 v156, v156, v244
	v_sub_f32_e32 v244, v157, v245
	v_exp_f32_e64 v245, -|v159|
	v_fma_f32 v157, v156, s40, 0
	v_fmamk_f32 v156, v244, 0x3d800000, v157
	v_add_f32_e32 v244, 1.0, v246
	v_log_f32_e32 v244, v244
	v_add_f32_e32 v245, 1.0, v245
	v_log_f32_e32 v245, v245
	v_min_f32_e32 v158, 0, v158
	v_sub_f32_e32 v158, v158, v244
	v_min_f32_e32 v159, 0, v159
	v_sub_f32_e32 v244, v159, v245
	v_fmamk_f32 v159, v158, 0x3d800000, v156
	v_fmamk_f32 v158, v244, 0x3d800000, v159
	ds_bpermute_b32 v247, v164, v148
	ds_bpermute_b32 v248, v164, v140
	ds_bpermute_b32 v249, v164, v134
	ds_bpermute_b32 v131, v164, v158
	s_waitcnt lgkmcnt(0)
	v_add_f32_e32 v247, v148, v247
	v_add_f32_e32 v248, v140, v248
	v_add_f32_e32 v249, v134, v249
	v_add_f32_e32 v131, v158, v131
	v_cndmask_b32_e64 v165, v247, v148, s[0:1]
	v_cndmask_b32_e64 v240, v248, v140, s[0:1]
	v_cndmask_b32_e64 v242, v249, v134, s[0:1]
	v_cndmask_b32_e64 v164, v131, v158, s[0:1]
	ds_bpermute_b32 v247, v239, v165
	ds_bpermute_b32 v248, v239, v240
	ds_bpermute_b32 v249, v239, v242
	ds_bpermute_b32 v131, v239, v164
	s_waitcnt lgkmcnt(0)
	v_add_f32_e32 v166, v165, v247
	v_add_f32_e32 v241, v240, v248
	v_add_f32_e32 v243, v242, v249
	v_add_f32_e32 v239, v164, v131
	s_and_saveexec_b64 s[28:29], s[10:11]
	ds_write_b32 v167, v166
	ds_write_b32 v167, v241 offset:64
	ds_write_b32 v167, v243 offset:128
	ds_write_b32 v167, v239 offset:192
	s_or_b64 exec, exec, s[28:29]
	v_cndmask_b32_e64 v167, v242, v243, s[8:9]
	v_sub_f32_e32 v242, v167, v134
	v_cndmask_b32_e64 v167, v240, v241, s[8:9]
	v_cndmask_b32_e64 v165, v165, v166, s[8:9]
	v_cndmask_b32_e64 v164, v164, v239, s[8:9]
	v_sub_f32_e32 v240, v167, v140
	v_sub_f32_e32 v166, v165, v148
	v_sub_f32_e32 v164, v164, v158
	v_pk_add_f32 v[132:133], v[132:133], v[242:243] op_sel_hi:[1,0]
	v_pk_add_f32 v[134:135], v[134:135], v[242:243] op_sel_hi:[1,0]
	v_pk_add_f32 v[136:137], v[136:137], v[240:241] op_sel_hi:[1,0]
	v_pk_add_f32 v[140:141], v[140:141], v[240:241] op_sel_hi:[1,0]
	v_pk_add_f32 v[144:145], v[144:145], v[166:167] op_sel_hi:[1,0]
	v_pk_add_f32 v[148:149], v[148:149], v[166:167] op_sel_hi:[1,0]
	v_pk_add_f32 v[156:157], v[156:157], v[164:165] op_sel_hi:[1,0]
	v_pk_add_f32 v[158:159], v[158:159], v[164:165] op_sel_hi:[1,0]
.LBB0_1182:
	s_waitcnt lgkmcnt(0)
	s_barrier
	s_andn2_b64 vcc, exec, s[2:3]
	s_cbranch_vccnz .LBB0_1144
	ds_read2st64_b32 v[166:167], v187 offset1:1
	ds_read2st64_b32 v[164:165], v187 offset0:2 offset1:3
	s_waitcnt lgkmcnt(1)
	v_add_f32_e32 v166, 0, v166
	v_add_f32_e32 v239, v166, v167
	s_waitcnt lgkmcnt(0)
	v_add_f32_e32 v239, v239, v164
	v_add_f32_e32 v239, v239, v165
	v_exp_f32_e32 v239, v239
	s_and_saveexec_b64 s[2:3], s[12:13]
	ds_write_b32 v188, v239
	s_or_b64 exec, exec, s[2:3]
	v_cndmask_b32_e64 v166, 0, v166, s[14:15]
	v_cndmask_b32_e64 v167, 0, v167, s[16:17]
	v_add_f32_e32 v166, v166, v167
	v_cndmask_b32_e64 v164, 0, v164, s[18:19]
	v_add_f32_e32 v164, v166, v164
	v_cndmask_b32_e64 v165, 0, v165, s[20:21]
	v_add_f32_e32 v164, v164, v165
	v_add_f32_e32 v165, v145, v164
	v_exp_f32_e64 v167, -v165
	v_exp_f32_e32 v165, v165
	s_waitcnt vmcnt(36)
	v_lshlrev_b32_e32 v166, 16, v35
	v_mul_f32_e32 v166, 0x3e000000, v166
	s_waitcnt vmcnt(35)
	v_lshlrev_b32_e32 v240, 16, v190
	v_mul_f32_e32 v165, v166, v165
	v_mul_f32_e32 v167, v167, v240
	v_cvt_pk_bf16_f32 v165, v165, s0
	v_add_u32_e32 v166, s41, v197
	ds_write_b16 v166, v165
	v_cvt_pk_bf16_f32 v165, v167, s0
	v_add_u32_e32 v166, s42, v197
	ds_write_b16 v166, v165
	v_mul_f32_e32 v165, v239, v167
	v_cvt_pk_bf16_f32 v165, v165, s0
	v_add_u32_e32 v166, s43, v197
	ds_write_b16 v166, v165
	v_add_f32_e32 v165, v144, v164
	v_exp_f32_e64 v167, -v165
	v_exp_f32_e32 v165, v165
	s_waitcnt vmcnt(34)
	v_lshlrev_b32_e32 v166, 16, v214
	v_mul_f32_e32 v166, 0x3e000000, v166
	s_waitcnt vmcnt(33)
	v_lshlrev_b32_e32 v240, 16, v215
	v_mul_f32_e32 v165, v166, v165
	v_mul_f32_e32 v167, v167, v240
	v_cvt_pk_bf16_f32 v165, v165, s0
	v_add_u32_e32 v166, s41, v198
	ds_write_b16 v166, v165
	v_cvt_pk_bf16_f32 v165, v167, s0
	v_add_u32_e32 v166, s42, v198
	ds_write_b16 v166, v165
	v_mul_f32_e32 v165, v239, v167
	v_cvt_pk_bf16_f32 v165, v165, s0
	v_add_u32_e32 v166, s43, v198
	ds_write_b16 v166, v165
	v_add_f32_e32 v165, v149, v164
	v_exp_f32_e64 v167, -v165
	v_exp_f32_e32 v165, v165
	s_waitcnt vmcnt(32)
	v_lshlrev_b32_e32 v166, 16, v222
	v_mul_f32_e32 v166, 0x3e000000, v166
	s_waitcnt vmcnt(31)
	v_lshlrev_b32_e32 v240, 16, v223
	v_mul_f32_e32 v165, v166, v165
	v_mul_f32_e32 v167, v167, v240
	v_cvt_pk_bf16_f32 v165, v165, s0
	v_add_u32_e32 v166, s41, v199
	ds_write_b16 v166, v165
	v_cvt_pk_bf16_f32 v165, v167, s0
	v_add_u32_e32 v166, s42, v199
	ds_write_b16 v166, v165
	v_mul_f32_e32 v165, v239, v167
	v_cvt_pk_bf16_f32 v165, v165, s0
	v_add_u32_e32 v166, s43, v199
	v_add_f32_e32 v164, v148, v164
	ds_write_b16 v166, v165
	v_exp_f32_e64 v166, -v164
	v_exp_f32_e32 v164, v164
	s_waitcnt vmcnt(30)
	v_lshlrev_b32_e32 v165, 16, v231
	v_mul_f32_e32 v165, 0x3e000000, v165
	s_waitcnt vmcnt(29)
	v_lshlrev_b32_e32 v167, 16, v232
	global_load_ushort v35, v66, s[64:65]
	global_load_ushort v190, v68, s[64:65]
	global_load_ushort v214, v82, s[64:65]
	global_load_ushort v215, v84, s[64:65]
	global_load_ushort v222, v100, s[64:65]
	global_load_ushort v223, v102, s[64:65]
	global_load_ushort v231, v116, s[64:65]
	global_load_ushort v232, v118, s[64:65]
	v_mul_f32_e32 v164, v165, v164
	v_cvt_pk_bf16_f32 v164, v164, s0
	v_add_u32_e32 v165, s41, v200
	ds_write_b16 v165, v164
	ds_read2_b32 v[164:165], v187 offset0:16 offset1:80
	v_mul_f32_e32 v240, v166, v167
	ds_read2_b32 v[166:167], v187 offset0:144 offset1:208
	v_cvt_pk_bf16_f32 v241, v240, s0
	v_mul_f32_e32 v240, v239, v240
	s_waitcnt lgkmcnt(1)
	v_add_f32_e32 v164, 0, v164
	v_add_f32_e32 v239, v164, v165
	s_waitcnt lgkmcnt(0)
	v_add_f32_e32 v239, v239, v166
	v_add_f32_e32 v239, v239, v167
	v_exp_f32_e32 v239, v239
	v_add_u32_e32 v242, s42, v200
	ds_write_b16 v242, v241
	v_cvt_pk_bf16_f32 v240, v240, s0
	v_add_u32_e32 v241, s43, v200
	ds_write_b16 v241, v240
	s_and_saveexec_b64 s[2:3], s[12:13]
	ds_write_b32 v188, v239 offset:64
	s_or_b64 exec, exec, s[2:3]
	v_cndmask_b32_e64 v164, 0, v164, s[14:15]
	v_cndmask_b32_e64 v165, 0, v165, s[16:17]
	v_add_f32_e32 v164, v164, v165
	v_cndmask_b32_e64 v165, 0, v166, s[18:19]
	v_add_f32_e32 v164, v164, v165
	v_cndmask_b32_e64 v165, 0, v167, s[20:21]
	v_add_f32_e32 v164, v164, v165
	v_add_f32_e32 v165, v137, v164
	v_exp_f32_e64 v167, -v165
	v_exp_f32_e32 v165, v165
	s_waitcnt vmcnt(36)
	v_lshlrev_b32_e32 v166, 16, v191
	v_mul_f32_e32 v166, 0x3e000000, v166
	s_waitcnt vmcnt(35)
	v_lshlrev_b32_e32 v240, 16, v192
	v_mul_f32_e32 v165, v166, v165
	v_mul_f32_e32 v167, v167, v240
	v_cvt_pk_bf16_f32 v165, v165, s0
	v_add_u32_e32 v166, s41, v201
	ds_write_b16 v166, v165
	v_cvt_pk_bf16_f32 v165, v167, s0
	v_add_u32_e32 v166, s42, v201
	ds_write_b16 v166, v165
	v_mul_f32_e32 v165, v239, v167
	v_cvt_pk_bf16_f32 v165, v165, s0
	v_add_u32_e32 v166, s43, v201
	ds_write_b16 v166, v165
	v_add_f32_e32 v165, v136, v164
	v_exp_f32_e64 v167, -v165
	v_exp_f32_e32 v165, v165
	s_waitcnt vmcnt(34)
	v_lshlrev_b32_e32 v166, 16, v216
	v_mul_f32_e32 v166, 0x3e000000, v166
	s_waitcnt vmcnt(33)
	v_lshlrev_b32_e32 v240, 16, v217
	v_mul_f32_e32 v165, v166, v165
	v_mul_f32_e32 v167, v167, v240
	v_cvt_pk_bf16_f32 v165, v165, s0
	v_add_u32_e32 v166, s41, v202
	ds_write_b16 v166, v165
	v_cvt_pk_bf16_f32 v165, v167, s0
	v_add_u32_e32 v166, s42, v202
	ds_write_b16 v166, v165
	v_mul_f32_e32 v165, v239, v167
	v_cvt_pk_bf16_f32 v165, v165, s0
	v_add_u32_e32 v166, s43, v202
	ds_write_b16 v166, v165
	v_add_f32_e32 v165, v141, v164
	v_exp_f32_e64 v167, -v165
	v_exp_f32_e32 v165, v165
	s_waitcnt vmcnt(32)
	v_lshlrev_b32_e32 v166, 16, v224
	v_mul_f32_e32 v166, 0x3e000000, v166
	s_waitcnt vmcnt(31)
	v_lshlrev_b32_e32 v240, 16, v225
	v_mul_f32_e32 v165, v166, v165
	v_mul_f32_e32 v167, v167, v240
	v_cvt_pk_bf16_f32 v165, v165, s0
	v_add_u32_e32 v166, s41, v203
	ds_write_b16 v166, v165
	v_cvt_pk_bf16_f32 v165, v167, s0
	v_add_u32_e32 v166, s42, v203
	ds_write_b16 v166, v165
	v_mul_f32_e32 v165, v239, v167
	v_cvt_pk_bf16_f32 v165, v165, s0
	v_add_u32_e32 v166, s43, v203
	v_add_f32_e32 v164, v140, v164
	ds_write_b16 v166, v165
	v_exp_f32_e64 v166, -v164
	v_exp_f32_e32 v164, v164
	s_waitcnt vmcnt(30)
	v_lshlrev_b32_e32 v165, 16, v233
	v_mul_f32_e32 v165, 0x3e000000, v165
	s_waitcnt vmcnt(29)
	v_lshlrev_b32_e32 v167, 16, v234
	global_load_ushort v191, v70, s[64:65]
	global_load_ushort v192, v72, s[64:65]
	global_load_ushort v216, v88, s[64:65]
	global_load_ushort v217, v90, s[64:65]
	global_load_ushort v224, v104, s[64:65]
	global_load_ushort v225, v106, s[64:65]
	global_load_ushort v233, v120, s[64:65]
	global_load_ushort v234, v122, s[64:65]
	v_mul_f32_e32 v164, v165, v164
	v_cvt_pk_bf16_f32 v164, v164, s0
	v_add_u32_e32 v165, s41, v204
	ds_write_b16 v165, v164
	ds_read2_b32 v[164:165], v187 offset0:32 offset1:96
	v_mul_f32_e32 v240, v166, v167
	ds_read2_b32 v[166:167], v187 offset0:160 offset1:224
	v_cvt_pk_bf16_f32 v241, v240, s0
	v_mul_f32_e32 v240, v239, v240
	s_waitcnt lgkmcnt(1)
	v_add_f32_e32 v164, 0, v164
	v_add_f32_e32 v239, v164, v165
	s_waitcnt lgkmcnt(0)
	v_add_f32_e32 v239, v239, v166
	v_add_f32_e32 v239, v239, v167
	v_exp_f32_e32 v239, v239
	v_add_u32_e32 v242, s42, v204
	ds_write_b16 v242, v241
	v_cvt_pk_bf16_f32 v240, v240, s0
	v_add_u32_e32 v241, s43, v204
	ds_write_b16 v241, v240
	s_and_saveexec_b64 s[2:3], s[12:13]
	ds_write_b32 v188, v239 offset:128
	s_or_b64 exec, exec, s[2:3]
	v_cndmask_b32_e64 v164, 0, v164, s[14:15]
	v_cndmask_b32_e64 v165, 0, v165, s[16:17]
	v_add_f32_e32 v164, v164, v165
	v_cndmask_b32_e64 v165, 0, v166, s[18:19]
	v_add_f32_e32 v164, v164, v165
	v_cndmask_b32_e64 v165, 0, v167, s[20:21]
	v_add_f32_e32 v164, v164, v165
	v_add_f32_e32 v165, v133, v164
	v_exp_f32_e64 v167, -v165
	v_exp_f32_e32 v165, v165
	s_waitcnt vmcnt(36)
	v_lshlrev_b32_e32 v166, 16, v193
	v_mul_f32_e32 v166, 0x3e000000, v166
	s_waitcnt vmcnt(35)
	v_lshlrev_b32_e32 v240, 16, v194
	v_mul_f32_e32 v165, v166, v165
	v_mul_f32_e32 v167, v167, v240
	v_cvt_pk_bf16_f32 v165, v165, s0
	v_add_u32_e32 v166, s41, v205
	ds_write_b16 v166, v165
	v_cvt_pk_bf16_f32 v165, v167, s0
	v_add_u32_e32 v166, s42, v205
	ds_write_b16 v166, v165
	v_mul_f32_e32 v165, v239, v167
	v_cvt_pk_bf16_f32 v165, v165, s0
	v_add_u32_e32 v166, s43, v205
	ds_write_b16 v166, v165
	v_add_f32_e32 v165, v132, v164
	v_exp_f32_e64 v167, -v165
	v_exp_f32_e32 v165, v165
	s_waitcnt vmcnt(34)
	v_lshlrev_b32_e32 v166, 16, v218
	v_mul_f32_e32 v166, 0x3e000000, v166
	s_waitcnt vmcnt(33)
; __device__ __forceinline__ void gla_fast_unit(int unit, const bf16_t* P, const float* w_up, const float* b_up, float* Of, float* Ob, LAS unsigned char* lds0) {
;     ...
;         GLA_LOAD(0, graw0, qr0, kr0, vraw0);
;         for (int cidx = -1; cidx < NCH + 1; cidx += 2) {
;             GLA_PREP(cidx, graw0, qr0, kr0, vraw0, graw0, qr0, kr0, vraw0);
;             GLA_PREP(cidx + 1, graw0, qr0, kr0, vraw0, graw0, qr0, kr0, vraw0);
;         }
	v_lshlrev_b32_e32 v240, 16, v219
	v_mul_f32_e32 v165, v166, v165
	v_mul_f32_e32 v167, v167, v240
	v_cvt_pk_bf16_f32 v165, v165, s0
	v_add_u32_e32 v166, s41, v206
	ds_write_b16 v166, v165
	v_cvt_pk_bf16_f32 v165, v167, s0
	v_add_u32_e32 v166, s42, v206
	ds_write_b16 v166, v165
	v_mul_f32_e32 v165, v239, v167
	v_cvt_pk_bf16_f32 v165, v165, s0
	v_add_u32_e32 v166, s43, v206
	ds_write_b16 v166, v165
	v_add_f32_e32 v165, v135, v164
	v_exp_f32_e64 v167, -v165
	v_exp_f32_e32 v165, v165
	s_waitcnt vmcnt(32)
	v_lshlrev_b32_e32 v166, 16, v226
	v_mul_f32_e32 v166, 0x3e000000, v166
	s_waitcnt vmcnt(31)
	v_lshlrev_b32_e32 v240, 16, v227
	v_mul_f32_e32 v165, v166, v165
	v_mul_f32_e32 v167, v167, v240
	v_cvt_pk_bf16_f32 v165, v165, s0
	v_add_u32_e32 v166, s41, v207
	ds_write_b16 v166, v165
	v_cvt_pk_bf16_f32 v165, v167, s0
	v_add_u32_e32 v166, s42, v207
	ds_write_b16 v166, v165
	v_mul_f32_e32 v165, v239, v167
	v_cvt_pk_bf16_f32 v165, v165, s0
	v_add_u32_e32 v166, s43, v207
	v_add_f32_e32 v164, v134, v164
	ds_write_b16 v166, v165
	v_exp_f32_e64 v166, -v164
	v_exp_f32_e32 v164, v164
	s_waitcnt vmcnt(30)
	v_lshlrev_b32_e32 v165, 16, v235
	v_mul_f32_e32 v165, 0x3e000000, v165
	s_waitcnt vmcnt(29)
	v_lshlrev_b32_e32 v167, 16, v236
	global_load_ushort v193, v74, s[64:65]
	global_load_ushort v194, v76, s[64:65]
	global_load_ushort v218, v92, s[64:65]
	global_load_ushort v219, v94, s[64:65]
	global_load_ushort v226, v108, s[64:65]
	global_load_ushort v227, v110, s[64:65]
	global_load_ushort v235, v124, s[64:65]
	global_load_ushort v236, v126, s[64:65]
	v_mul_f32_e32 v164, v165, v164
	v_cvt_pk_bf16_f32 v164, v164, s0
	v_add_u32_e32 v165, s41, v208
	ds_write_b16 v165, v164
	ds_read2_b32 v[164:165], v187 offset0:48 offset1:112
	v_mul_f32_e32 v240, v166, v167
	ds_read2_b32 v[166:167], v187 offset0:176 offset1:240
	v_cvt_pk_bf16_f32 v241, v240, s0
	v_mul_f32_e32 v240, v239, v240
	s_waitcnt lgkmcnt(1)
	v_add_f32_e32 v239, 0, v164
	v_add_f32_e32 v164, v239, v165
	s_waitcnt lgkmcnt(0)
	v_add_f32_e32 v164, v164, v166
	v_add_f32_e32 v164, v164, v167
	v_exp_f32_e32 v164, v164
	v_add_u32_e32 v242, s42, v208
	ds_write_b16 v242, v241
	v_cvt_pk_bf16_f32 v240, v240, s0
	v_add_u32_e32 v241, s43, v208
	ds_write_b16 v241, v240
	s_and_saveexec_b64 s[2:3], s[12:13]
	ds_write_b32 v188, v164 offset:192
	s_or_b64 exec, exec, s[2:3]
	v_cndmask_b32_e64 v239, 0, v239, s[14:15]
	v_cndmask_b32_e64 v165, 0, v165, s[16:17]
	v_add_f32_e32 v165, v239, v165
	v_cndmask_b32_e64 v166, 0, v166, s[18:19]
	v_add_f32_e32 v165, v165, v166
	v_cndmask_b32_e64 v166, 0, v167, s[20:21]
	v_add_f32_e32 v165, v165, v166
	v_add_f32_e32 v166, v157, v165
	v_exp_f32_e64 v239, -v166
	v_exp_f32_e32 v166, v166
	s_waitcnt vmcnt(36)
	v_lshlrev_b32_e32 v167, 16, v195
	v_mul_f32_e32 v167, 0x3e000000, v167
	s_waitcnt vmcnt(35)
	v_lshlrev_b32_e32 v240, 16, v196
	v_mul_f32_e32 v166, v167, v166
	v_mul_f32_e32 v239, v239, v240
	v_cvt_pk_bf16_f32 v166, v166, s0
	v_add_u32_e32 v167, s41, v209
	ds_write_b16 v167, v166
	v_cvt_pk_bf16_f32 v166, v239, s0
	v_add_u32_e32 v167, s42, v209
	ds_write_b16 v167, v166
	v_mul_f32_e32 v166, v164, v239
	v_cvt_pk_bf16_f32 v166, v166, s0
	v_add_u32_e32 v167, s43, v209
	ds_write_b16 v167, v166
	v_add_f32_e32 v166, v156, v165
	v_exp_f32_e64 v239, -v166
	v_exp_f32_e32 v166, v166
	s_waitcnt vmcnt(34)
	v_lshlrev_b32_e32 v167, 16, v220
	v_mul_f32_e32 v167, 0x3e000000, v167
	s_waitcnt vmcnt(33)
	v_lshlrev_b32_e32 v240, 16, v221
	v_mul_f32_e32 v166, v167, v166
	v_mul_f32_e32 v239, v239, v240
	v_cvt_pk_bf16_f32 v166, v166, s0
	v_add_u32_e32 v167, s41, v210
	ds_write_b16 v167, v166
	v_cvt_pk_bf16_f32 v166, v239, s0
	v_add_u32_e32 v167, s42, v210
	ds_write_b16 v167, v166
	v_mul_f32_e32 v166, v164, v239
	v_cvt_pk_bf16_f32 v166, v166, s0
	v_add_u32_e32 v167, s43, v210
	ds_write_b16 v167, v166
	v_add_f32_e32 v166, v159, v165
	v_exp_f32_e64 v239, -v166
	v_exp_f32_e32 v166, v166
	s_waitcnt vmcnt(32)
	v_lshlrev_b32_e32 v167, 16, v229
	v_mul_f32_e32 v167, 0x3e000000, v167
	s_waitcnt vmcnt(31)
	v_lshlrev_b32_e32 v240, 16, v230
	v_mul_f32_e32 v166, v167, v166
	v_mul_f32_e32 v239, v239, v240
	v_cvt_pk_bf16_f32 v166, v166, s0
	v_add_u32_e32 v167, s41, v211
	ds_write_b16 v167, v166
	v_cvt_pk_bf16_f32 v166, v239, s0
	v_add_u32_e32 v167, s42, v211
	ds_write_b16 v167, v166
	v_mul_f32_e32 v166, v164, v239
	v_cvt_pk_bf16_f32 v166, v166, s0
	v_add_u32_e32 v167, s43, v211
	v_add_f32_e32 v165, v158, v165
	ds_write_b16 v167, v166
	v_exp_f32_e64 v167, -v165
	v_exp_f32_e32 v165, v165
	s_waitcnt vmcnt(30)
	v_lshlrev_b32_e32 v166, 16, v237
	v_mul_f32_e32 v166, 0x3e000000, v166
	s_waitcnt vmcnt(29)
	v_lshlrev_b32_e32 v239, 16, v238
	global_load_ushort v195, v78, s[64:65]
	global_load_ushort v196, v80, s[64:65]
	global_load_ushort v220, v96, s[64:65]
	global_load_ushort v221, v98, s[64:65]
	global_load_ushort v229, v112, s[64:65]
	global_load_ushort v230, v114, s[64:65]
	global_load_ushort v237, v128, s[64:65]
	global_load_ushort v238, v130, s[64:65]
	v_mul_f32_e32 v165, v166, v165
	v_mul_f32_e32 v167, v167, v239
	v_cvt_pk_bf16_f32 v165, v165, s0
	v_add_u32_e32 v166, s41, v212
	ds_write_b16 v166, v165
	v_cvt_pk_bf16_f32 v165, v167, s0
	v_add_u32_e32 v166, s42, v212
	v_mul_f32_e32 v164, v164, v167
	ds_write_b16 v166, v165
	v_cvt_pk_bf16_f32 v164, v164, s0
	v_add_u32_e32 v165, s43, v212
	ds_write_b16 v165, v164
	v_add_u32_e32 v164, v189, v185
	s_waitcnt vmcnt(36)
	ds_write_b128 v164, v[40:43]
	v_add_u32_e32 v164, v189, v171
	s_waitcnt vmcnt(35)
	ds_write_b128 v164, v[44:47]
	v_add_u32_e32 v164, v189, v186
	s_waitcnt vmcnt(34)
	ds_write_b128 v164, v[48:51]
	v_add_u32_e32 v164, v189, v172
	s_waitcnt vmcnt(33)
	ds_write_b128 v164, v[52:55]
	global_load_dwordx4 v[40:43], v58, s[64:65]
	global_load_dwordx4 v[44:47], v60, s[64:65]
	global_load_dwordx4 v[48:51], v62, s[64:65]
	global_load_dwordx4 v[52:55], v64, s[64:65]
	s_branch .LBB0_1144
.LBB0_1198:
	s_setprio 0
	s_waitcnt vmcnt(0)
	s_mov_b64 s[2:3], 0
